# stats epilogue: tree select (depth 3) with lane masks hoisted to kernel entry
# baseline (speedup 1.0000x reference)
_Z9k2_layer1PKfS0_S0_PfS1_S1_:
	s_load_dwordx8 s[4:11], s[0:1], 0x0
	s_load_dwordx4 s[12:15], s[0:1], 0x20
	s_lshr_b32 s16, s2, 5
	s_and_b32 s17, s2, 31
	s_lshl_b32 s17, s17, 4
	s_movk_i32 s18, 0x500
	v_and_b32_e32 v1, 15, v0
	v_lshrrev_b32_e32 v2, 4, v0
	v_lshl_add_u32 v3, s16, 4, v2
	v_add_u32_e32 v4, s17, v1
	v_lshlrev_b32_e32 v4, 2, v4
	v_lshl_add_u32 v5, v3, 11, v4
	v_add_u32_e32 v6, 0x40000, v5
	v_lshl_add_u32 v7, v3, 14, v4
	v_add_u32_e32 v7, 0x80000, v7
	v_add_u32_e32 v8, 0x1000, v7
	v_add_u32_e32 v9, 0x2000, v7
	v_add_u32_e32 v10, 0x3000, v7
	v_and_b32_e32 v11, 7, v1
	v_lshl_add_u32 v11, v3, 3, v11
	v_lshlrev_b32_e32 v11, 2, v11
	v_and_b32_e32 v12, 8, v1
	v_lshl_add_u32 v11, v12, 9, v11
	v_add_u32_e32 v11, 0x280000, v11
	v_lshrrev_b32_e32 v13, 6, v0
	v_bfe_u32 v14, v0, 4, 2
	v_lshl_add_u32 v15, v13, 4, v1
	v_mul_u32_u24_e32 v16, 20, v15
	v_mad_u32_u24 v16, v14, s18, v16
	v_add_u32_e32 v17, 0x1400, v16
	v_add_u32_e32 v18, 0x2800, v16
	v_add_u32_e32 v19, 0x3c00, v16
	v_lshlrev_b32_e32 v20, 2, v15
	s_lshl_b32 s19, s2, 4
	v_add_u32_e32 v59, s19, v1
	v_lshlrev_b32_e32 v59, 6, v59
	v_lshl_add_u32 v59, v13, 4, v59
	v_lshl_add_u32 v59, v14, 2, v59
	v_lshlrev_b32_e32 v59, 2, v59
	v_and_b32_e32 v90, 3, v1
	v_lshl_add_u32 v90, v14, 2, v90
	v_lshl_add_u32 v90, v13, 4, v90
	s_lshl_b32 s19, s16, 8
	s_and_b32 s20, s2, 1
	s_mul_i32 s20, s20, 0x3000
	s_add_u32 s19, s19, s20
	v_lshl_add_u32 v90, v90, 2, s19
	s_waitcnt lgkmcnt(0)
	global_load_dword v24, v5, s[4:5]
	global_load_dword v25, v6, s[4:5]
	global_load_dword v26, v7, s[4:5]
	global_load_dword v27, v7, s[4:5] offset:2048
	global_load_dword v28, v8, s[4:5]
	global_load_dword v29, v8, s[4:5] offset:2048
	global_load_dword v30, v9, s[4:5]
	global_load_dword v31, v9, s[4:5] offset:2048
	global_load_dword v32, v10, s[4:5]
	global_load_dword v33, v10, s[4:5] offset:2048
	global_load_dword v34, v11, s[4:5]
	global_load_dwordx4 v[36:39], v16, s[6:7]
	global_load_dwordx4 v[40:43], v17, s[6:7]
	global_load_dwordx4 v[44:47], v18, s[6:7]
	global_load_dwordx4 v[48:51], v19, s[6:7]
	global_load_dword v52, v16, s[6:7] offset:16
	global_load_dword v53, v17, s[6:7] offset:16
	global_load_dword v54, v18, s[6:7] offset:16
	global_load_dword v55, v19, s[6:7] offset:16
	global_load_dword v56, v20, s[8:9]
	v_lshlrev_b32_e32 v21, 2, v0
	v_and_b32_e32 v22, 63, v0
	v_lshlrev_b32_e32 v22, 2, v22
	v_lshlrev_b32_e32 v23, 2, v14
	v_add_u32_e32 v23, 0xc00, v23
	v_lshlrev_b32_e32 v57, 3, v12
	v_lshl_add_u32 v57, v2, 2, v57
	v_add_u32_e32 v57, 0xc00, v57
	v_mul_u32_u24_e32 v58, 0x900000, v12
	v_sub_u32_e32 v58, 0x3b000000, v58
	v_mov_b32_e32 v89, 1.0
	s_mov_b32 s20, 0x01010101
	s_mov_b32 s21, 0x01010101
	s_mov_b32 s30, 0xaaaaaaaa
	s_mov_b32 s31, 0xaaaaaaaa
	s_mov_b32 s32, 0xcccccccc
	s_mov_b32 s33, 0xcccccccc
	s_mov_b32 s34, 0xf0f0f0f0
	s_mov_b32 s35, 0xf0f0f0f0
	s_mov_b32 s36, 0x000f000f
	s_mov_b32 s37, 0x000f000f
	s_mov_b32 s38, 0x00f000f0
	s_mov_b32 s39, 0x00f000f0
	s_mov_b32 s22, 0xffff
	s_mov_b32 s23, 0
	s_waitcnt vmcnt(9)
	v_add_f32_dpp v34, v34, v34 quad_perm:[1,0,3,2] row_mask:0xf bank_mask:0xf
	v_add_f32_e32 v26, v26, v27
	v_add_f32_e32 v28, v28, v29
	v_add_f32_dpp v34, v34, v34 quad_perm:[2,3,0,1] row_mask:0xf bank_mask:0xf
	v_add_f32_e32 v30, v30, v31
	v_add_f32_e32 v32, v32, v33
	v_add_f32_dpp v34, v34, v34 row_half_mirror row_mask:0xf bank_mask:0xf
	v_add_f32_e32 v26, v26, v28
	v_add_f32_e32 v30, v30, v32
	v_mul_f32_e32 v25, 0x3b000000, v25
	v_add_f32_e32 v26, v26, v30
	v_mul_f32_e32 v34, v58, v34
	v_mul_f32_e32 v26, 0x3b000000, v26
	ds_write_b32 v21, v24
	ds_write_b32 v21, v25 offset:1024
	ds_write_b32 v21, v26 offset:2048
	s_mov_b64 exec, s[20:21]
	ds_write_b32 v57, v34
	s_mov_b64 exec, -1
	s_waitcnt lgkmcnt(0)
	s_barrier
	ds_read2st64_b32 v[60:61], v22 offset0:0 offset1:1
	ds_read2st64_b32 v[62:63], v22 offset0:2 offset1:3
	ds_read2st64_b32 v[64:65], v22 offset0:4 offset1:5
	ds_read2st64_b32 v[66:67], v22 offset0:6 offset1:7
	ds_read2st64_b32 v[68:69], v22 offset0:8 offset1:9
	ds_read2st64_b32 v[70:71], v22 offset0:10 offset1:11
	ds_read2_b32 v[72:73], v23 offset0:0 offset1:16
	ds_read2_b32 v[74:75], v23 offset0:4 offset1:20
	ds_read2_b32 v[76:77], v23 offset0:8 offset1:24
	ds_read2_b32 v[78:79], v23 offset0:12 offset1:28
	s_waitcnt vmcnt(0)
	s_waitcnt lgkmcnt(9)
	v_mfma_f32_16x16x4_f32 v[80:83], v36, v60, 0
	v_mfma_f32_16x16x4_f32 v[84:87], v40, v61, 0
	s_waitcnt lgkmcnt(8)
	v_mfma_f32_16x16x4_f32 v[80:83], v44, v62, v[80:83]
	v_mfma_f32_16x16x4_f32 v[84:87], v48, v63, v[84:87]
	s_waitcnt lgkmcnt(7)
	v_mfma_f32_16x16x4_f32 v[80:83], v38, v64, v[80:83]
	v_mfma_f32_16x16x4_f32 v[84:87], v42, v65, v[84:87]
	v_cndmask_b32_e64 v88, 0, v56, s[22:23]
	s_waitcnt lgkmcnt(6)
	v_mfma_f32_16x16x4_f32 v[80:83], v46, v66, v[80:83]
	v_mfma_f32_16x16x4_f32 v[84:87], v50, v67, v[84:87]
	s_waitcnt lgkmcnt(5)
	v_mfma_f32_16x16x4_f32 v[80:83], v39, v68, v[80:83]
	v_mfma_f32_16x16x4_f32 v[84:87], v43, v69, v[84:87]
	s_waitcnt lgkmcnt(4)
	v_mfma_f32_16x16x4_f32 v[80:83], v47, v70, v[80:83]
	v_mfma_f32_16x16x4_f32 v[84:87], v51, v71, v[84:87]
	s_waitcnt lgkmcnt(0)
	v_fmac_f32_e32 v88, v37, v72
	v_fmac_f32_e32 v88, v52, v73
	v_fmac_f32_e32 v88, v41, v74
	v_fmac_f32_e32 v88, v53, v75
	v_fmac_f32_e32 v88, v45, v76
	v_fmac_f32_e32 v88, v54, v77
	v_fmac_f32_e32 v88, v49, v78
	v_fmac_f32_e32 v88, v55, v79
	s_nop 1
	v_mfma_f32_16x16x4_f32 v[80:83], v88, v89, v[80:83]
	s_nop 7
	s_nop 1
	v_add_f32_e32 v80, v80, v84
	v_add_f32_e32 v81, v81, v85
	v_add_f32_e32 v82, v82, v86
	v_add_f32_e32 v83, v83, v87
	v_max_f32_e32 v80, 0, v80
	v_max_f32_e32 v81, 0, v81
	v_max_f32_e32 v82, 0, v82
	v_max_f32_e32 v83, 0, v83
	global_store_dwordx4 v59, v[80:83], s[10:11] sc1
	v_mul_f32_e32 v84, v80, v80
	v_mul_f32_e32 v85, v81, v81
	v_mul_f32_e32 v86, v82, v82
	v_mul_f32_e32 v87, v83, v83
	v_add_f32_dpp v80, v80, v80 quad_perm:[1,0,3,2] row_mask:0xf bank_mask:0xf
	v_add_f32_dpp v81, v81, v81 quad_perm:[1,0,3,2] row_mask:0xf bank_mask:0xf
	v_add_f32_dpp v82, v82, v82 quad_perm:[1,0,3,2] row_mask:0xf bank_mask:0xf
	v_add_f32_dpp v83, v83, v83 quad_perm:[1,0,3,2] row_mask:0xf bank_mask:0xf
	v_add_f32_dpp v84, v84, v84 quad_perm:[1,0,3,2] row_mask:0xf bank_mask:0xf
	v_add_f32_dpp v85, v85, v85 quad_perm:[1,0,3,2] row_mask:0xf bank_mask:0xf
	v_add_f32_dpp v86, v86, v86 quad_perm:[1,0,3,2] row_mask:0xf bank_mask:0xf
	v_add_f32_dpp v87, v87, v87 quad_perm:[1,0,3,2] row_mask:0xf bank_mask:0xf
	v_add_f32_dpp v80, v80, v80 quad_perm:[2,3,0,1] row_mask:0xf bank_mask:0xf
	v_add_f32_dpp v81, v81, v81 quad_perm:[2,3,0,1] row_mask:0xf bank_mask:0xf
	v_add_f32_dpp v82, v82, v82 quad_perm:[2,3,0,1] row_mask:0xf bank_mask:0xf
	v_add_f32_dpp v83, v83, v83 quad_perm:[2,3,0,1] row_mask:0xf bank_mask:0xf
	v_add_f32_dpp v84, v84, v84 quad_perm:[2,3,0,1] row_mask:0xf bank_mask:0xf
	v_add_f32_dpp v85, v85, v85 quad_perm:[2,3,0,1] row_mask:0xf bank_mask:0xf
	v_add_f32_dpp v86, v86, v86 quad_perm:[2,3,0,1] row_mask:0xf bank_mask:0xf
	v_add_f32_dpp v87, v87, v87 quad_perm:[2,3,0,1] row_mask:0xf bank_mask:0xf
	v_add_f32_dpp v80, v80, v80 row_half_mirror row_mask:0xf bank_mask:0xf
	v_add_f32_dpp v81, v81, v81 row_half_mirror row_mask:0xf bank_mask:0xf
	v_add_f32_dpp v82, v82, v82 row_half_mirror row_mask:0xf bank_mask:0xf
	v_add_f32_dpp v83, v83, v83 row_half_mirror row_mask:0xf bank_mask:0xf
	v_add_f32_dpp v84, v84, v84 row_half_mirror row_mask:0xf bank_mask:0xf
	v_add_f32_dpp v85, v85, v85 row_half_mirror row_mask:0xf bank_mask:0xf
	v_add_f32_dpp v86, v86, v86 row_half_mirror row_mask:0xf bank_mask:0xf
	v_add_f32_dpp v87, v87, v87 row_half_mirror row_mask:0xf bank_mask:0xf
	v_add_f32_dpp v80, v80, v80 row_mirror row_mask:0xf bank_mask:0xf
	v_add_f32_dpp v81, v81, v81 row_mirror row_mask:0xf bank_mask:0xf
	v_add_f32_dpp v82, v82, v82 row_mirror row_mask:0xf bank_mask:0xf
	v_add_f32_dpp v83, v83, v83 row_mirror row_mask:0xf bank_mask:0xf
	v_add_f32_dpp v84, v84, v84 row_mirror row_mask:0xf bank_mask:0xf
	v_add_f32_dpp v85, v85, v85 row_mirror row_mask:0xf bank_mask:0xf
	v_add_f32_dpp v86, v86, v86 row_mirror row_mask:0xf bank_mask:0xf
	v_add_f32_dpp v87, v87, v87 row_mirror row_mask:0xf bank_mask:0xf
	v_cndmask_b32_e64 v80, v80, v81, s[30:31]
	v_cndmask_b32_e64 v82, v82, v83, s[30:31]
	v_cndmask_b32_e64 v84, v84, v85, s[30:31]
	v_cndmask_b32_e64 v86, v86, v87, s[30:31]
	v_cndmask_b32_e64 v80, v80, v82, s[32:33]
	v_cndmask_b32_e64 v84, v84, v86, s[32:33]
	v_cndmask_b32_e64 v80, v80, v84, s[34:35]
	s_mov_b64 exec, s[36:37]
	global_atomic_add_f32 v90, v80, s[12:13]
	s_mov_b64 exec, s[38:39]
	global_atomic_add_f32 v90, v80, s[14:15]
	s_endpgm

	.amdhsa_kernel _Z9k2_layer1PKfS0_S0_PfS1_S1_
		.amdhsa_group_segment_fixed_size 3712
		.amdhsa_private_segment_fixed_size 0
		.amdhsa_kernarg_size 48
		.amdhsa_user_sgpr_count 2
		.amdhsa_user_sgpr_dispatch_ptr 0
		.amdhsa_user_sgpr_queue_ptr 0
		.amdhsa_user_sgpr_kernarg_segment_ptr 1
		.amdhsa_user_sgpr_dispatch_id 0
		.amdhsa_user_sgpr_kernarg_preload_length 0
		.amdhsa_user_sgpr_kernarg_preload_offset 0
		.amdhsa_user_sgpr_private_segment_size 0
		.amdhsa_uses_dynamic_stack 0
		.amdhsa_enable_private_segment 0
		.amdhsa_system_sgpr_workgroup_id_x 1
		.amdhsa_system_sgpr_workgroup_id_y 0
		.amdhsa_system_sgpr_workgroup_id_z 0
		.amdhsa_system_sgpr_workgroup_info 0
		.amdhsa_system_vgpr_workitem_id 0
		.amdhsa_next_free_vgpr 92
		.amdhsa_next_free_sgpr 40
		.amdhsa_accum_offset 92
		.amdhsa_reserve_vcc 1
		.amdhsa_float_round_mode_32 0
		.amdhsa_float_round_mode_16_64 0
		.amdhsa_float_denorm_mode_32 3
		.amdhsa_float_denorm_mode_16_64 3
		.amdhsa_dx10_clamp 1
		.amdhsa_ieee_mode 1
		.amdhsa_fp16_overflow 0
		.amdhsa_tg_split 0
		.amdhsa_exception_fp_ieee_invalid_op 0
		.amdhsa_exception_fp_denorm_src 0
		.amdhsa_exception_fp_ieee_div_zero 0
		.amdhsa_exception_fp_ieee_overflow 0
		.amdhsa_exception_fp_ieee_underflow 0
		.amdhsa_exception_fp_ieee_inexact 0
		.amdhsa_exception_int_div_zero 0
	.end_amdhsa_kernel

_Z7k_layerPKfS0_S0_S0_S0_S0_S0_PfS1_S1_:
	s_load_dwordx4 s[28:31], s[0:1], 0x40
	s_mov_b32 s36, 0xaaaaaaaa
	s_mov_b32 s37, 0xaaaaaaaa
	s_mov_b32 s38, 0xcccccccc
	s_mov_b32 s39, 0xcccccccc
	s_mov_b32 s40, 0xf0f0f0f0
	s_mov_b32 s41, 0xf0f0f0f0
	s_mov_b32 s42, 0x000f000f
	s_mov_b32 s43, 0x000f000f
	s_mov_b32 s44, 0x00f000f0
	s_mov_b32 s45, 0x00f000f0
	s_load_dwordx2 s[10:11], s[0:1], 0x0
	s_load_dwordx4 s[12:15], s[0:1], 0x28
	s_load_dwordx2 s[8:9], s[0:1], 0x38
	v_cmp_lt_u32_e64 s[6:7], 63, v0
	v_cmp_gt_u32_e64 s[4:5], 64, v0
	v_mov_b32_e32 v70, 0x7fc00000
	v_lshlrev_b32_e32 v18, 2, v0
	s_and_saveexec_b64 s[16:17], s[4:5]
	s_cbranch_execz .LBB2_2
	s_load_dwordx8 s[20:27], s[0:1], 0x8
	s_waitcnt lgkmcnt(0)
	v_add_u32_e32 v77, 0x3000, v18
	global_load_dword v81, v77, s[20:21] offset:256 sc1
	global_load_dword v80, v77, s[22:23] offset:256 sc1
	global_load_dword v83, v77, s[20:21] offset:512 sc1
	global_load_dword v82, v77, s[22:23] offset:512 sc1
	global_load_dword v85, v77, s[20:21] offset:768 sc1
	global_load_dword v84, v77, s[22:23] offset:768 sc1
	global_load_dword v87, v77, s[20:21] offset:1024 sc1
	global_load_dword v86, v77, s[22:23] offset:1024 sc1
	global_load_dword v89, v77, s[20:21] offset:1280 sc1
	global_load_dword v88, v77, s[22:23] offset:1280 sc1
	global_load_dword v91, v77, s[20:21] offset:1536 sc1
	global_load_dword v90, v77, s[22:23] offset:1536 sc1
	global_load_dword v93, v77, s[20:21] offset:1792 sc1
	global_load_dword v92, v77, s[22:23] offset:1792 sc1
	global_load_dword v95, v77, s[20:21] sc1
	global_load_dword v94, v77, s[22:23] sc1
	global_load_dword v48, v18, s[20:21] sc1
	global_load_dword v1, v18, s[22:23] sc1
	global_load_dword v73, v18, s[20:21] offset:256 sc1
	global_load_dword v72, v18, s[22:23] offset:256 sc1
	global_load_dword v69, v18, s[20:21] offset:512 sc1
	global_load_dword v68, v18, s[22:23] offset:512 sc1
	global_load_dword v67, v18, s[20:21] offset:768 sc1
	global_load_dword v66, v18, s[22:23] offset:768 sc1
	global_load_dword v65, v18, s[20:21] offset:1024 sc1
	global_load_dword v64, v18, s[22:23] offset:1024 sc1
	global_load_dword v63, v18, s[20:21] offset:1280 sc1
	global_load_dword v62, v18, s[22:23] offset:1280 sc1
	global_load_dword v61, v18, s[20:21] offset:1536 sc1
	global_load_dword v60, v18, s[22:23] offset:1536 sc1
	global_load_dword v53, v18, s[20:21] offset:1792 sc1
	global_load_dword v52, v18, s[22:23] offset:1792 sc1
	global_load_dword v49, v18, s[24:25]
	global_load_dword v76, v18, s[26:27]
	s_waitcnt vmcnt(16)
	v_add_f32_e32 v70, 0, v1

.LBB2_4:
	s_or_b64 exec, exec, s[2:3]
	v_lshlrev_b32_e32 v23, 2, v23
	s_waitcnt lgkmcnt(0)
	s_barrier
	s_waitcnt vmcnt(25)
	ds_read_b128 v[60:63], v23 offset:512
	ds_read_b128 v[64:67], v23 offset:528
	v_cmp_eq_u32_e32 vcc, 0, v75
	s_and_b32 s9, s9, 0xffff
	s_mov_b32 s11, 0x20000
	s_waitcnt vmcnt(16) lgkmcnt(1)
	v_mul_f32_e32 v48, v58, v60
	s_waitcnt vmcnt(0)
	v_cndmask_b32_e32 v20, 0, v20, vcc
	s_mov_b32 s10, 0x100000
	v_mfma_f32_16x16x4_f32 a[0:3], v48, v14, 0
	v_mul_f32_e32 v14, v56, v61
	v_cmp_eq_u32_e32 vcc, 0, v19
	s_nop 0
	v_mfma_f32_16x16x4_f32 a[4:7], v14, v15, 0
	v_mul_f32_e32 v14, v54, v62
	s_nop 1
	v_mfma_f32_16x16x4_f32 a[0:3], v14, v16, a[0:3]
	v_mul_f32_e32 v14, v50, v63
	s_nop 1
	v_mfma_f32_16x16x4_f32 a[4:7], v14, v17, a[4:7]
	s_waitcnt lgkmcnt(0)
	v_mul_f32_e32 v14, v46, v64
	s_nop 1
	v_mfma_f32_16x16x4_f32 a[0:3], v14, v10, a[0:3]
	v_mul_f32_e32 v10, v44, v65
	ds_read_b128 v[14:17], v23 offset:1024
	ds_read_b128 v[60:63], v23 offset:768
	ds_read_b128 v[68:71], v23 offset:1040
	ds_read_b128 v[76:79], v23 offset:784
	v_mfma_f32_16x16x4_f32 a[4:7], v10, v11, a[4:7]
	v_mul_f32_e32 v11, v42, v66
	s_waitcnt lgkmcnt(3)
	v_mul_f32_e32 v10, v59, v14
	s_waitcnt lgkmcnt(2)
	v_fmac_f32_e32 v10, v58, v60
	v_mul_f32_e32 v14, v57, v15
	v_add_f32_e32 v10, v20, v10
	v_fmac_f32_e32 v14, v56, v61
	v_add_f32_e32 v10, v14, v10
	v_mfma_f32_16x16x4_f32 a[0:3], v11, v12, a[0:3]
	v_mul_f32_e32 v11, v55, v16
	v_mul_f32_e32 v12, v36, v67
	v_fmac_f32_e32 v11, v54, v62
	ds_read_b128 v[52:55], v23 offset:544
	v_add_f32_e32 v14, v11, v10
	v_mul_f32_e32 v15, v51, v17
	v_fmac_f32_e32 v15, v50, v63
	v_mfma_f32_16x16x4_f32 a[4:7], v12, v13, a[4:7]
	ds_read_b128 v[10:13], v23 offset:560
	s_waitcnt lgkmcnt(1)
	v_mul_f32_e32 v16, v40, v52
	v_add_f32_e32 v14, v15, v14
	v_mul_f32_e32 v15, v47, v68
	v_fmac_f32_e32 v15, v46, v76
	v_add_f32_e32 v14, v14, v15
	v_mul_f32_e32 v15, v38, v53
	v_mfma_f32_16x16x4_f32 a[0:3], v16, v6, a[0:3]
	v_mul_f32_e32 v20, v34, v54
	v_mul_f32_e32 v6, v45, v69
	v_fmac_f32_e32 v6, v44, v77
	v_add_f32_e32 v6, v6, v14
	v_mul_f32_e32 v14, v43, v70
	v_fmac_f32_e32 v14, v42, v78
	v_add_f32_e32 v6, v14, v6
	v_mfma_f32_16x16x4_f32 a[4:7], v15, v7, a[4:7]
	ds_read_b128 v[14:17], v23 offset:800
	ds_read_b128 v[42:45], v23 offset:1056
	v_mul_f32_e32 v7, v37, v71
	v_fmac_f32_e32 v7, v36, v79
	v_add_f32_e32 v48, v7, v6
	v_mov_b32_e32 v6, v40
	v_mov_b32_e32 v40, v41
	v_mov_b32_e32 v41, v39
	v_mfma_f32_16x16x4_f32 a[0:3], v20, v8, a[0:3]
	v_mul_f32_e32 v8, v32, v55
	v_mov_b32_e32 v7, v38
	s_waitcnt lgkmcnt(0)
	v_mul_f32_e64 v46, v40, v42
	v_mul_f32_e64 v47, v41, v43
	v_mul_f32_e32 v11, v28, v11
	v_pk_fma_f32 v[6:7], v[6:7], v[14:15], v[46:47]
	ds_read_b128 v[36:39], v23 offset:1072
	ds_read_b128 v[40:43], v23 offset:816
	v_mfma_f32_16x16x4_f32 a[4:7], v8, v9, a[4:7]
	v_mul_f32_e32 v8, v30, v10
	v_add_f32_e32 v6, v48, v6
	v_add_f32_e32 v10, v7, v6
	v_mov_b32_e32 v7, v32
	v_mov_b32_e32 v32, v35
	v_mov_b32_e32 v6, v34
	v_mov_b32_e32 v23, v21
	v_mfma_f32_16x16x4_f32 a[0:3], v8, v2, a[0:3]
	v_mul_f32_e64 v8, v32, v44
	v_mul_f32_e64 v9, v33, v45
	v_mov_b32_e32 v20, 0
	v_fma_f32 v6, v6, v16, v8
	v_fma_f32 v7, v7, v17, v9
	v_mul_f32_e32 v9, v24, v12
	v_add_f32_e32 v2, v6, v10
	v_add_f32_e32 v8, v7, v2
	v_mov_b32_e32 v2, v30
	v_mfma_f32_16x16x4_f32 a[4:7], v11, v3, a[4:7]
	v_mov_b32_e32 v3, v28
	v_mov_b32_e32 v28, v31
	s_waitcnt lgkmcnt(1)
	v_mul_f32_e64 v6, v28, v36
	v_mul_f32_e64 v7, v29, v37
	v_mov_b32_e32 v16, v21
	s_waitcnt lgkmcnt(0)
	v_pk_fma_f32 v[2:3], v[2:3], v[40:41], v[6:7]
	v_mov_b32_e32 v17, v21
	v_add_f32_e32 v2, v8, v2
	v_mfma_f32_16x16x4_f32 a[0:3], v9, v4, a[0:3]
	v_add_f32_e32 v4, v3, v2
	v_mul_f32_e32 v8, v26, v13
	v_mov_b32_e32 v3, v26
	v_mov_b32_e32 v26, v25
	v_mov_b32_e32 v2, v24
	v_pk_mul_f32 v[6:7], v[26:27], v[38:39]
	v_mov_b32_e32 v9, v21
	v_pk_fma_f32 v[2:3], v[2:3], v[42:43], v[6:7]
	v_mfma_f32_16x16x4_f32 a[4:7], v8, v5, a[4:7]
	v_add_f32_e32 v2, v2, v4
	v_add_f32_e32 v4, v3, v2
	v_mov_b32_e32 v5, 1.0
	v_mov_b32_e32 v8, v21
	s_nop 0
	v_mfma_f32_16x16x4_f32 a[0:3], v4, v5, a[0:3]
	s_nop 3
	v_accvgpr_read_b32 v3, a7
	v_accvgpr_read_b32 v2, a6
	v_accvgpr_read_b32 v7, a5
	v_accvgpr_read_b32 v6, a4
	s_nop 1
	v_accvgpr_read_b32 v5, a3
	v_accvgpr_read_b32 v4, a2
	v_pk_add_f32 v[2:3], v[2:3], v[4:5]
	v_accvgpr_read_b32 v5, a1
	v_accvgpr_read_b32 v4, a0
	v_pk_add_f32 v[4:5], v[6:7], v[4:5]
	v_max_f32_e32 v14, 0, v2
	v_max_f32_e32 v12, 0, v4
	v_max_f32_e32 v13, 0, v5
	v_max_f32_e32 v15, 0, v3
	v_lshlrev_b32_e32 v2, 6, v22
	v_and_b32_e32 v3, 12, v1
	v_or3_b32 v2, v2, v74, v3
	v_lshlrev_b32_e32 v2, 2, v2
	buffer_store_dwordx4 v[12:15], v2, s[8:11], 0 offen sc1
	v_mul_f32_e32 v4, v12, v12
	v_mul_f32_e32 v5, v13, v13
	v_mul_f32_e32 v6, v14, v14
	v_mul_f32_e32 v7, v15, v15
	v_and_b32_e32 v8, 3, v19
	v_and_b32_e32 v9, 12, v1
	v_or3_b32 v8, v8, v9, v74
	s_lshl_b32 s2, s12, 8
	s_bfe_u32 s3, s16, 0x10004
	s_mul_i32 s3, s3, 0x3000
	s_add_u32 s2, s2, s3
	v_lshl_add_u32 v8, v8, 2, s2
	v_add_f32_dpp v12, v12, v12 quad_perm:[1,0,3,2] row_mask:0xf bank_mask:0xf
	v_add_f32_dpp v13, v13, v13 quad_perm:[1,0,3,2] row_mask:0xf bank_mask:0xf
	v_add_f32_dpp v14, v14, v14 quad_perm:[1,0,3,2] row_mask:0xf bank_mask:0xf
	v_add_f32_dpp v15, v15, v15 quad_perm:[1,0,3,2] row_mask:0xf bank_mask:0xf
	v_add_f32_dpp v4, v4, v4 quad_perm:[1,0,3,2] row_mask:0xf bank_mask:0xf
	v_add_f32_dpp v5, v5, v5 quad_perm:[1,0,3,2] row_mask:0xf bank_mask:0xf
	v_add_f32_dpp v6, v6, v6 quad_perm:[1,0,3,2] row_mask:0xf bank_mask:0xf
	v_add_f32_dpp v7, v7, v7 quad_perm:[1,0,3,2] row_mask:0xf bank_mask:0xf
	v_add_f32_dpp v12, v12, v12 quad_perm:[2,3,0,1] row_mask:0xf bank_mask:0xf
	v_add_f32_dpp v13, v13, v13 quad_perm:[2,3,0,1] row_mask:0xf bank_mask:0xf
	v_add_f32_dpp v14, v14, v14 quad_perm:[2,3,0,1] row_mask:0xf bank_mask:0xf
	v_add_f32_dpp v15, v15, v15 quad_perm:[2,3,0,1] row_mask:0xf bank_mask:0xf
	v_add_f32_dpp v4, v4, v4 quad_perm:[2,3,0,1] row_mask:0xf bank_mask:0xf
	v_add_f32_dpp v5, v5, v5 quad_perm:[2,3,0,1] row_mask:0xf bank_mask:0xf
	v_add_f32_dpp v6, v6, v6 quad_perm:[2,3,0,1] row_mask:0xf bank_mask:0xf
	v_add_f32_dpp v7, v7, v7 quad_perm:[2,3,0,1] row_mask:0xf bank_mask:0xf
	v_add_f32_dpp v12, v12, v12 row_half_mirror row_mask:0xf bank_mask:0xf
	v_add_f32_dpp v13, v13, v13 row_half_mirror row_mask:0xf bank_mask:0xf
	v_add_f32_dpp v14, v14, v14 row_half_mirror row_mask:0xf bank_mask:0xf
	v_add_f32_dpp v15, v15, v15 row_half_mirror row_mask:0xf bank_mask:0xf
	v_add_f32_dpp v4, v4, v4 row_half_mirror row_mask:0xf bank_mask:0xf
	v_add_f32_dpp v5, v5, v5 row_half_mirror row_mask:0xf bank_mask:0xf
	v_add_f32_dpp v6, v6, v6 row_half_mirror row_mask:0xf bank_mask:0xf
	v_add_f32_dpp v7, v7, v7 row_half_mirror row_mask:0xf bank_mask:0xf
	v_add_f32_dpp v12, v12, v12 row_mirror row_mask:0xf bank_mask:0xf
	v_add_f32_dpp v13, v13, v13 row_mirror row_mask:0xf bank_mask:0xf
	v_add_f32_dpp v14, v14, v14 row_mirror row_mask:0xf bank_mask:0xf
	v_add_f32_dpp v15, v15, v15 row_mirror row_mask:0xf bank_mask:0xf
	v_add_f32_dpp v4, v4, v4 row_mirror row_mask:0xf bank_mask:0xf
	v_add_f32_dpp v5, v5, v5 row_mirror row_mask:0xf bank_mask:0xf
	v_add_f32_dpp v6, v6, v6 row_mirror row_mask:0xf bank_mask:0xf
	v_add_f32_dpp v7, v7, v7 row_mirror row_mask:0xf bank_mask:0xf
	v_cndmask_b32_e64 v12, v12, v13, s[36:37]
	v_cndmask_b32_e64 v14, v14, v15, s[36:37]
	v_cndmask_b32_e64 v4, v4, v5, s[36:37]
	v_cndmask_b32_e64 v6, v6, v7, s[36:37]
	v_cndmask_b32_e64 v12, v12, v14, s[38:39]
	v_cndmask_b32_e64 v4, v4, v6, s[38:39]
	v_cndmask_b32_e64 v12, v12, v4, s[40:41]
	s_mov_b64 exec, s[42:43]
	global_atomic_add_f32 v8, v12, s[28:29]
	s_mov_b64 exec, s[44:45]
	global_atomic_add_f32 v8, v12, s[30:31]
	s_endpgm

	.amdhsa_kernel _Z7k_layerPKfS0_S0_S0_S0_S0_S0_PfS1_S1_
		.amdhsa_group_segment_fixed_size 1280
		.amdhsa_private_segment_fixed_size 0
		.amdhsa_kernarg_size 80
		.amdhsa_user_sgpr_count 2
		.amdhsa_user_sgpr_dispatch_ptr 0
		.amdhsa_user_sgpr_queue_ptr 0
		.amdhsa_user_sgpr_kernarg_segment_ptr 1
		.amdhsa_user_sgpr_dispatch_id 0
		.amdhsa_user_sgpr_kernarg_preload_length 0
		.amdhsa_user_sgpr_kernarg_preload_offset 0
		.amdhsa_user_sgpr_private_segment_size 0
		.amdhsa_uses_dynamic_stack 0
		.amdhsa_enable_private_segment 0
		.amdhsa_system_sgpr_workgroup_id_x 1
		.amdhsa_system_sgpr_workgroup_id_y 0
		.amdhsa_system_sgpr_workgroup_id_z 0
		.amdhsa_system_sgpr_workgroup_info 0
		.amdhsa_system_vgpr_workitem_id 0
		.amdhsa_next_free_vgpr 104
		.amdhsa_next_free_sgpr 46
		.amdhsa_accum_offset 96
		.amdhsa_reserve_vcc 1
		.amdhsa_float_round_mode_32 0
		.amdhsa_float_round_mode_16_64 0
		.amdhsa_float_denorm_mode_32 3
		.amdhsa_float_denorm_mode_16_64 3
		.amdhsa_dx10_clamp 1
		.amdhsa_ieee_mode 1
		.amdhsa_fp16_overflow 0
		.amdhsa_tg_split 0
		.amdhsa_exception_fp_ieee_invalid_op 0
		.amdhsa_exception_fp_denorm_src 0
		.amdhsa_exception_fp_ieee_div_zero 0
		.amdhsa_exception_fp_ieee_overflow 0
		.amdhsa_exception_fp_ieee_underflow 0
		.amdhsa_exception_fp_ieee_inexact 0
		.amdhsa_exception_int_div_zero 0
	.end_amdhsa_kernel
